# mixer: k rows double-buffered in the unused LDS hole, fetched two chunks ahead with counted vmcnt (on top of v13)
# baseline (speedup 1.0000x reference)
.LBB0_446:
	v_readlane_b32 s0, v254, 8
	v_mov_b32_e32 v2, v0
	v_readlane_b32 s1, v254, 9
	s_andn2_b64 vcc, exec, s[0:1]
	v_readfirstlane_b32 s0, v2
	s_cbranch_vccnz .LBB0_483
	v_and_b32_e32 v3, 63, v2
	v_lshlrev_b32_e32 v4, 1, v3
	v_and_b32_e32 v1, 62, v4
	v_cvt_f32_ubyte0_e32 v6, v1
	v_mul_f32_e32 v8, 0xbe549a78, v6
	s_mov_b32 s1, 0xc2fc0000
	v_cmp_gt_f32_e32 vcc, s1, v8
	v_or_b32_e32 v1, 1, v1
	v_cvt_f32_ubyte0_e32 v1, v1
	v_cndmask_b32_e32 v8, 0, v251, vcc
	v_fmac_f32_e32 v8, 0xbe549a78, v6
	v_exp_f32_e32 v6, v8
	v_mul_f32_e32 v8, 0xbe549a78, v1
	v_cmp_gt_f32_e64 s[40:41], s1, v8
	s_movk_i32 s1, 0x1100
	v_cmp_gt_i32_e64 s[4:5], s1, v2
	v_cndmask_b32_e64 v8, 0, v251, s[40:41]
	v_fmac_f32_e32 v8, 0xbe549a78, v1
	v_exp_f32_e32 v8, v8
	v_cndmask_b32_e32 v1, 0, v252, vcc
	v_ldexp_f32 v1, v6, v1
	v_cndmask_b32_e64 v6, 0, v252, s[40:41]
	v_writelane_b32 v255, s4, 34
	s_add_u32 s26, s22, 0x2e300000
	v_ldexp_f32 v94, v8, v6
	v_cvt_f32_i32_e32 v6, v2
	v_writelane_b32 v255, s5, 35
	v_cmp_gt_i32_e64 s[4:5], 64, v2
	s_addc_u32 s27, s23, 0
	s_ashr_i32 s2, s0, 6
	v_writelane_b32 v255, s4, 36
	v_readlane_b32 s1, v254, 47
	v_lshlrev_b32_e32 v104, 2, v3
	v_writelane_b32 v255, s5, 37
	v_add_u32_e32 v102, s1, v4
	s_lshl_b32 s1, s2, 9
	s_add_i32 s4, 0, 0x1a000
	s_add_i32 s17, s4, s1
	v_add_u32_e32 v108, 0, v104
	s_movk_i32 s1, 0x11c
	v_add_f32_e32 v96, 0xc1f80000, v6
	v_sub_f32_e32 v97, 0x41f80000, v6
	v_add_f32_e32 v98, 1.0, v6
	v_sub_f32_e32 v99, 0x427c0000, v6
	s_lshl_b32 s95, s2, 3
	v_bfe_u32 v6, v2, 3, 3
	v_mad_u32_u24 v11, v3, s1, v108
	v_and_b32_e32 v12, 48, v2
	s_lshl_b32 s1, s2, 5
	v_readlane_b32 s35, v254, 51
	v_and_b32_e32 v7, 15, v2
	v_or_b32_e32 v100, s95, v6
	v_lshlrev_b32_e32 v6, 3, v2
	s_lshl_b32 s16, s2, 10
	s_lshl_b32 s5, s2, 4
	s_and_b32 s6, s0, 0xffffffc0
	v_add_u32_e32 v13, s4, v12
	s_add_i32 s4, s1, s35
	v_bfe_u32 v5, v2, 4, 2
	v_lshlrev_b32_e32 v194, 4, v7
	v_and_b32_e32 v6, 56, v6
	s_cmp_lt_u32 s0, 64
	v_lshl_add_u64 v[38:39], s[26:27], 0, v[194:195]
	v_lshlrev_b32_e32 v194, 1, v6
	s_cselect_b64 s[36:37], -1, 0
	s_and_b32 s1, s1, 32
	v_lshlrev_b32_e32 v17, 2, v5
	v_lshl_add_u64 v[40:41], s[26:27], 0, v[194:195]
	v_readlane_b32 s8, v254, 50
	v_lshlrev_b32_e32 v194, 3, v5
	v_or_b32_e32 v109, s1, v7
	v_or_b32_e32 v18, s1, v17
	s_or_b32 s1, s1, 16
	v_mov_b32_e32 v8, s8
	s_movk_i32 s7, 0x90
	v_add_u32_e32 v14, s4, v194
	s_ashr_i32 s4, s0, 3
	v_or_b32_e32 v21, s1, v17
	v_cmp_gt_u32_e32 vcc, 32, v3
	v_lshlrev_b32_e32 v103, 3, v3
	v_mad_u32_u24 v3, v3, s7, v8
	v_bfi_b32 v8, -16, s4, v2
	v_or_b32_e32 v19, 2, v18
	v_or_b32_e32 v22, 2, v21
	s_and_b32 s0, s4, -16
	s_movk_i32 s4, 0x110
	v_cmp_gt_i32_e64 s[48:49], v19, v8
	v_or_b32_e32 v19, 3, v18
	v_readlane_b32 s10, v254, 52
	v_cmp_gt_i32_e64 s[56:57], v22, v8
	v_or_b32_e32 v22, 3, v21
	v_mul_lo_u32 v9, v8, s4
	v_cmp_gt_i32_e64 s[44:45], v18, v8
	v_cmp_lt_i32_e64 s[46:47], v18, v8
	v_cmp_gt_i32_e64 s[50:51], v19, v8
	v_mul_lo_u32 v19, v8, s7
	v_cmp_gt_i32_e64 s[52:53], v21, v8
	v_cmp_lt_i32_e64 s[54:55], v21, v8
	v_cmp_gt_i32_e64 s[58:59], v22, v8
	v_mov_b32_e32 v8, s10
	v_or_b32_e32 v23, s1, v7
	s_ashr_i32 s1, s0, 31
	v_mad_u32_u24 v22, v109, s7, v8
	v_mad_u32_u24 v24, v23, s7, v8
	v_or_b32_e32 v8, s5, v7
	s_lshl_b64 s[0:1], s[0:1], 1
	v_mul_lo_u32 v8, v8, s7
	s_add_u32 s0, s22, s0
	v_add_u32_e32 v25, 0, v8
	v_or_b32_e32 v8, s5, v17
	s_addc_u32 s1, s23, s1
	v_readlane_b32 s9, v254, 48
	v_readlane_b32 s24, v254, 49
	v_add_u32_e32 v15, 0, v9
	v_mad_u32_u24 v16, v109, s4, 0
	v_add_u32_e32 v26, s35, v9
	v_mad_u32_u24 v23, v23, s4, 0
	v_lshlrev_b32_e32 v17, 2, v8
	v_lshl_add_u64 v[8:9], s[0:1], 0, v[194:195]
	s_mov_b64 s[0:1], 0x36700000
	s_lshl_b32 s94, s2, 11
	s_or_b32 s4, s95, 4
	v_add_u32_e32 v20, s10, v19
	v_add_u32_e32 v19, s8, v19
	v_add_u32_e32 v27, s8, v12
	v_lshl_add_u64 v[42:43], v[8:9], 0, s[0:1]
	s_add_i32 s19, s9, s94
	s_mov_b32 s8, s82
	s_add_i32 s82, s24, s94
	s_lshl_b32 s7, s4, 8
	s_or_b32 s83, s94, 0x100
	s_or_b32 s18, s94, 0x200
	s_or_b32 s14, s94, 0x300
	s_or_b32 s13, s94, 0x400
	s_or_b32 s33, s94, 0x500
	s_or_b32 s25, s94, 0x600
	s_or_b32 s10, s94, 0x700
	s_lshl_b32 s0, s4, 7
	s_cmp_gt_i32 s2, 0
	s_cselect_b64 s[60:61], -1, 0
	s_cmp_gt_i32 s2, 1
	s_cselect_b64 s[62:63], -1, 0
	s_cmp_gt_i32 s2, 2
	s_cselect_b64 s[64:65], -1, 0
	s_cmp_gt_i32 s2, 3
	s_cselect_b64 s[66:67], -1, 0
	s_cmp_gt_i32 s2, 4
	s_cselect_b64 s[68:69], -1, 0
	s_cmp_gt_i32 s2, 5
	v_lshlrev_b32_e32 v10, 4, v2
	s_cselect_b64 s[70:71], -1, 0
	s_cmp_gt_i32 s2, 6
	s_cselect_b64 s[72:73], -1, 0
	s_cmp_gt_i32 s2, 7
	v_add_u32_e32 v116, 0xfffffe00, v2
	v_lshl_add_u32 v117, v2, 2, s35
	v_add_u32_e32 v2, 0, v10
	v_xor_b32_e32 v107, 0x80, v104
	v_lshlrev_b32_e32 v18, 1, v18
	v_lshlrev_b32_e32 v21, 1, v21
	v_or_b32_e32 v110, s95, v5
	v_or_b32_e32 v112, s4, v5
	s_cselect_b64 s[74:75], -1, 0
	s_lshl_b32 s88, s2, 7
	s_or_b32 s90, s95, 1
	v_mul_u32_u24_e32 v5, 0x110, v7
	v_mul_u32_u24_e32 v7, 0x90, v7
	v_add_u32_e32 v122, 0x1b200, v2
	v_add_u32_e32 v2, 0, v17
	v_cndmask_b32_e64 v95, 1.0, -1.0, vcc
	v_sub_u32_e32 v101, 0x7ff, v100
	v_add_u32_e32 v105, s9, v104
	v_add_u32_e32 v106, s24, v104
	v_sub_u32_e32 v111, 0x7ff, v110
	v_sub_u32_e32 v113, 0x7ff, v112
	v_add_u32_e32 v114, s9, v107
	v_add_u32_e32 v115, s24, v107
	v_mov_b32_e32 v243, v106
	v_mov_b32_e32 v244, v115
	s_mul_i32 s1, s2, 0x880
	s_lshl_b32 s89, s90, 4
	s_mulk_i32 s90, 0x110
	s_or_b32 s91, s88, 32
	s_or_b32 s28, s88, 48
	s_lshl_b32 s29, s4, 4
	s_or_b32 s96, s88, 0x50
	s_or_b32 s42, s88, 0x60
	s_or_b32 s43, s88, 0x70
	s_sub_i32 s35, 0, s95
	v_sub_u32_e32 v118, 0, v109
	v_add_u32_e32 v119, 64, v100
	v_sub_u32_e32 v120, 0x7bf, v100
	v_sub_u32_e32 v121, 0, v110
	v_lshlrev_b32_e32 v194, 2, v4
	v_lshlrev_b32_e32 v44, 1, v6
	v_add_u32_e32 v123, s5, v11
	v_add_u32_e32 v124, s5, v3
	v_add_u32_e32 v125, s6, v13
	v_add_u32_e32 v126, v14, v5
	v_add_u32_e32 v127, v15, v12
	v_add_u32_e32 v128, v16, v12
	v_add_u32_e32 v129, v20, v18
	v_add_u32_e32 v130, v20, v21
	v_add_u32_e32 v131, v19, v12
	v_add_u32_e32 v132, v22, v12
	v_add_u32_e32 v133, v24, v12
	v_add_u32_e32 v134, v25, v12
	v_add_u32_e32 v135, v26, v12
	v_add_u32_e32 v136, v23, v12
	v_add_u32_e32 v137, v27, v7
	v_add_u32_e32 v138, 0x1b000, v2
	s_add_i32 s92, s7, 0
	s_mov_b32 s93, s8
	s_branch .LBB0_449

.LBB0_464:
	s_ashr_i32 s8, s24, 2
	s_add_i32 s24, s8, s78
	s_lshl_b32 s8, s79, 7
	s_and_b64 s[78:79], s[76:77], exec
	s_movk_i32 s9, 0x1500
	s_cselect_b32 s9, s9, 0x1800
	s_and_b64 s[6:7], exec, s[6:7]
	s_cselect_b32 s6, 0x900, s9
	s_lshl_b32 s2, s2, 6
	s_and_b32 s40, s2, 64
	s_add_i32 s7, s81, s8
	s_or_b32 s78, s7, s40
	s_ashr_i32 s7, s5, 31
	s_lshr_b32 s7, s7, 30
	s_add_i32 s7, s5, s7
	s_and_b32 s7, s7, 0x1ffffc
	s_sub_i32 s5, s5, s7
	s_lshl_b32 s84, s5, 11
	v_cndmask_b32_e64 v3, v111, v110, s[76:77]
	v_add_u32_e32 v3, s84, v3
	s_add_i32 s2, s80, s8
	v_mad_i64_i32 v[4:5], s[80:81], v3, s20, v[38:39]
	s_add_i32 s6, s6, s8
	s_mov_b32 s7, s3
	s_lshl_b64 s[80:81], s[2:3], 1
	s_mov_b32 m0, s19
	v_lshl_add_u64 v[6:7], v[4:5], 0, s[80:81]
	s_lshl_b64 s[6:7], s[6:7], 1
	v_cndmask_b32_e64 v3, v113, v112, s[76:77]
	s_waitcnt vmcnt(0) lgkmcnt(0)
	s_barrier
	global_load_lds_dwordx4 v[6:7], off
	v_lshl_add_u64 v[4:5], v[4:5], 0, s[6:7]
	s_mov_b32 m0, s82
	v_add_u32_e32 v3, s84, v3
	global_load_lds_dwordx4 v[4:5], off
	v_mad_i64_i32 v[4:5], s[86:87], v3, s20, v[38:39]
	s_add_i32 s85, s92, 0x1b600
	v_lshl_add_u64 v[6:7], v[4:5], 0, s[80:81]
	s_mov_b32 m0, s85
	s_add_i32 s86, s92, 0x1f600
	global_load_lds_dwordx4 v[6:7], off
	v_lshl_add_u64 v[4:5], v[4:5], 0, s[6:7]
	s_mov_b32 m0, s86
	v_cndmask_b32_e64 v3, v101, v100, s[76:77]
	global_load_lds_dwordx4 v[4:5], off
	v_add_u32_e32 v3, s84, v3
	v_mov_b64_e32 v[4:5], s[26:27]
	s_mov_b32 s79, s3
	v_mad_i64_i32 v[4:5], vcc, v3, s20, v[4:5]
	s_lshl_b64 s[78:79], s[78:79], 1
	s_add_i32 s87, s16, 0
	v_lshl_add_u64 v[4:5], v[4:5], 0, s[78:79]
	v_mov_b32_e32 v45, v195
	s_add_i32 s87, s87, 0x23600
	v_lshl_add_u64 v[4:5], v[4:5], 0, v[44:45]
	s_mov_b32 m0, s87
	v_mul_f32_e32 v144, 0x42800000, v2
	global_load_lds_dwordx4 v[4:5], off
	v_mul_f32_e32 v2, 0x42000000, v2
	v_exp_f32_e32 v18, v2
	s_ashr_i32 s9, s8, 31
	s_waitcnt vmcnt(0)
	s_lshl_b32 s2, s4, 13
	v_mad_i64_i32 v[2:3], s[4:5], s24, v242, v[42:43]
	v_lshl_add_u64 v[2:3], s[8:9], 1, v[2:3]
	s_lshl_b32 s4, s40, 1
	s_mov_b32 s5, s3
	v_mov_b32_e32 v22, 0
	v_lshl_add_u64 v[52:53], v[40:41], 0, s[78:79]
	v_sub_f32_e32 v45, 1.0, v140
	v_sub_f32_e32 v143, 1.0, v139
	v_lshl_add_u64 v[54:55], v[2:3], 0, s[4:5]
	v_mov_b32_e32 v47, v46
	s_mov_b32 s24, 0
	v_mov_b32_e32 v19, v18
	v_mov_b32_e32 v20, v18
	v_mov_b32_e32 v21, v18
	s_mov_b32 s4, 0
	v_mov_b32_e32 v23, v22
	v_mov_b32_e32 v24, v22
	v_mov_b32_e32 v25, v22
	v_mov_b32_e32 v26, v22
	v_mov_b32_e32 v27, v22
	v_mov_b32_e32 v28, v22
	v_mov_b32_e32 v29, v22
	v_mov_b32_e32 v30, v22
	v_mov_b32_e32 v31, v22
	v_mov_b32_e32 v32, v22
	v_mov_b32_e32 v33, v22
	v_mov_b32_e32 v34, v22
	v_mov_b32_e32 v35, v22
	v_mov_b32_e32 v36, v22
	v_mov_b32_e32 v37, v22
	v_add_u32_e32 v176, s4, v110
	v_add_u32_e32 v177, s24, v121
	v_add_u32_e32 v178, 64, v176
	v_add_u32_e32 v179, 0x7bf, v177
	v_cndmask_b32_e64 v178, v179, v178, s[76:77]
	v_add_u32_e32 v178, s84, v178
	v_mad_i64_i32 v[178:179], s[100:101], v178, s20, v[38:39]
	v_add_u32_e32 v176, 0x44, v176
	v_add_u32_e32 v180, 0x7bb, v177
	v_cndmask_b32_e64 v176, v180, v176, s[76:77]
	v_add_u32_e32 v176, s84, v176
	v_mad_i64_i32 v[180:181], s[100:101], v176, s20, v[38:39]
	v_lshl_add_u64 v[178:179], v[178:179], 0, s[6:7]
	v_lshl_add_u64 v[180:181], v[180:181], 0, s[6:7]
	s_add_i32 m0, s82, 0xfffe9200
	s_nop 0
	global_load_lds_dwordx4 v[178:179], off
	s_add_i32 m0, s86, 0xfffe9200
	s_nop 0
	global_load_lds_dwordx4 v[180:181], off
	s_waitcnt vmcnt(0) lgkmcnt(0)
	s_barrier
	s_branch .LBB0_466
.LBB0_465:
	s_waitcnt lgkmcnt(0)
	s_barrier
	ds_read_b128 v[10:13], v127
	ds_read_b128 v[14:17], v127 offset:64
	ds_read_b128 v[56:59], v127 offset:128
	ds_read_b128 v[60:63], v127 offset:192
	ds_read_b128 v[64:67], v128 offset:17408
	ds_read_b128 v[68:71], v128 offset:17472
	ds_read_b128 v[72:75], v128 offset:17536
	ds_read_b128 v[76:79], v128 offset:17600
	ds_read_b128 v[176:179], v128 offset:21760
	ds_read_b128 v[180:183], v128 offset:21824
	ds_read_b128 v[184:187], v128 offset:21888
	ds_read_b128 v[188:191], v128 offset:21952
	s_waitcnt lgkmcnt(7)
	v_mfma_f32_16x16x32_bf16 v[2:5], v[64:67], v[10:13], 0
	s_waitcnt lgkmcnt(6)
	v_mfma_f32_16x16x32_bf16 v[2:5], v[68:71], v[14:17], v[2:5]
	s_waitcnt lgkmcnt(3)
	v_mfma_f32_16x16x32_bf16 v[6:9], v[176:179], v[10:13], 0
	v_mfma_f32_16x16x32_bf16 v[2:5], v[72:75], v[56:59], v[2:5]
	s_waitcnt lgkmcnt(2)
	v_mfma_f32_16x16x32_bf16 v[6:9], v[180:183], v[14:17], v[6:9]
	v_mfma_f32_16x16x32_bf16 v[2:5], v[76:79], v[60:63], v[2:5]
	s_waitcnt lgkmcnt(1)
	v_mfma_f32_16x16x32_bf16 v[6:9], v[184:187], v[56:59], v[6:9]
	s_waitcnt lgkmcnt(0)
	v_mfma_f32_16x16x32_bf16 v[6:9], v[188:191], v[60:63], v[6:9]
	s_nop 6
	v_cndmask_b32_e64 v56, v2, 0, s[44:45]
	v_cndmask_b32_e64 v57, 0, v3, s[46:47]
	v_cndmask_b32_e64 v58, v4, 0, s[48:49]
	v_cndmask_b32_e64 v59, v5, 0, s[50:51]
	v_cvt_pk_bf16_f32 v56, v56, v57
	v_cvt_pk_bf16_f32 v57, v58, v59
	ds_write_b64 v129, v[56:57]
	v_cndmask_b32_e64 v6, v6, 0, s[52:53]
	v_cndmask_b32_e64 v7, 0, v7, s[54:55]
	v_cndmask_b32_e64 v8, v8, 0, s[56:57]
	v_cndmask_b32_e64 v9, v9, 0, s[58:59]
	v_cvt_pk_bf16_f32 v6, v6, v7
	v_cvt_pk_bf16_f32 v7, v8, v9
	ds_write_b64 v130, v[6:7]
	s_waitcnt lgkmcnt(0)
	s_barrier
	ds_read_b128 v[10:13], v131
	ds_read_b128 v[14:17], v132
	ds_read_b128 v[56:59], v133
	ds_read_b128 v[60:63], v131 offset:64
	ds_read_b128 v[64:67], v132 offset:64
	ds_read_b128 v[68:71], v133 offset:64
	ds_read_b128 v[72:75], v138
	ds_read_b128 v[76:79], v134 offset:52224
	ds_read_b128 v[176:179], v137
	ds_read_b128 v[180:183], v137 offset:2304
	ds_read_b128 v[184:187], v137 offset:4608
	ds_read_b128 v[188:191], v137 offset:6912
	ds_read_b128 v[200:203], v134 offset:52288
	ds_read_b128 v[204:207], v137 offset:64
	ds_read_b128 v[208:211], v137 offset:2368
	s_waitcnt lgkmcnt(13)
	v_mfma_f32_16x16x32_bf16 v[6:9], v[10:13], v[14:17], 0
	s_waitcnt lgkmcnt(12)
	v_mfma_f32_16x16x32_bf16 v[2:5], v[10:13], v[56:59], 0
	ds_read_b128 v[212:215], v137 offset:4672
	ds_read_b128 v[220:223], v137 offset:6976
	ds_read_b128 v[224:227], v135
	s_waitcnt lgkmcnt(13)
	v_mfma_f32_16x16x32_bf16 v[6:9], v[60:63], v[64:67], v[6:9]
	s_waitcnt lgkmcnt(12)
	v_mfma_f32_16x16x32_bf16 v[2:5], v[60:63], v[68:71], v[2:5]
	ds_read_b128 v[232:235], v128
	ds_read_b128 v[236:239], v136
	ds_read_b128 v[14:17], v135 offset:64
	s_waitcnt lgkmcnt(14)
	v_pk_mul_f32 v[22:23], v[22:23], v[72:73]
	v_pk_mul_f32 v[24:25], v[24:25], v[74:75]
	v_pk_mul_f32 v[26:27], v[26:27], v[72:73]
	v_pk_mul_f32 v[28:29], v[28:29], v[74:75]
	v_pk_mul_f32 v[30:31], v[30:31], v[72:73]
	v_pk_mul_f32 v[32:33], v[32:33], v[74:75]
	v_pk_mul_f32 v[34:35], v[34:35], v[72:73]
	v_pk_mul_f32 v[36:37], v[36:37], v[74:75]
	s_waitcnt lgkmcnt(12)
	v_mfma_f32_16x16x32_bf16 v[22:25], v[76:79], v[176:179], v[22:25]
	s_waitcnt lgkmcnt(11)
	v_mfma_f32_16x16x32_bf16 v[26:29], v[76:79], v[180:183], v[26:29]
	s_waitcnt lgkmcnt(10)
	v_mfma_f32_16x16x32_bf16 v[30:33], v[76:79], v[184:187], v[30:33]
	s_waitcnt lgkmcnt(9)
	v_mfma_f32_16x16x32_bf16 v[34:37], v[76:79], v[188:191], v[34:37]
	ds_read_b128 v[10:13], v128 offset:64
	ds_read_b128 v[56:59], v136 offset:64
	ds_read_b128 v[64:67], v135 offset:128
	ds_read_b128 v[60:63], v128 offset:128
	s_waitcnt lgkmcnt(11)
	v_mfma_f32_16x16x32_bf16 v[22:25], v[200:203], v[204:207], v[22:25]
	s_waitcnt lgkmcnt(10)
	v_mfma_f32_16x16x32_bf16 v[26:29], v[200:203], v[208:211], v[26:29]
	ds_read_b128 v[68:71], v136 offset:128
	ds_read_b128 v[72:75], v135 offset:192
	s_waitcnt lgkmcnt(11)
	v_mfma_f32_16x16x32_bf16 v[30:33], v[200:203], v[212:215], v[30:33]
	s_waitcnt lgkmcnt(10)
	v_mfma_f32_16x16x32_bf16 v[34:37], v[200:203], v[220:223], v[34:37]
	ds_read_b128 v[176:179], v128 offset:192
	ds_read_b128 v[180:183], v136 offset:192
	s_waitcnt lgkmcnt(10)
	v_mfma_f32_16x16x32_bf16 v[6:9], v[224:227], v[232:235], v[6:9]
	s_waitcnt lgkmcnt(9)
	v_mfma_f32_16x16x32_bf16 v[2:5], v[224:227], v[236:239], v[2:5]
	s_waitcnt lgkmcnt(7)
	v_mfma_f32_16x16x32_bf16 v[6:9], v[14:17], v[10:13], v[6:9]
	s_waitcnt lgkmcnt(6)
	v_mfma_f32_16x16x32_bf16 v[2:5], v[14:17], v[56:59], v[2:5]
	s_waitcnt lgkmcnt(4)
	v_mfma_f32_16x16x32_bf16 v[6:9], v[64:67], v[60:63], v[6:9]
	s_waitcnt lgkmcnt(3)
	v_mfma_f32_16x16x32_bf16 v[2:5], v[64:67], v[68:71], v[2:5]
	s_waitcnt lgkmcnt(1)
	v_mfma_f32_16x16x32_bf16 v[6:9], v[72:75], v[176:179], v[6:9]
	s_waitcnt lgkmcnt(0)
	v_mfma_f32_16x16x32_bf16 v[2:5], v[72:75], v[180:183], v[2:5]
	v_add_u32_e32 v57, s24, v118
	v_add_u32_e32 v56, s4, v109
	v_add_u32_e32 v58, 0x7ff, v57
	s_waitcnt vmcnt(2)
	s_cmpk_lt_i32 s4, 0x780
	s_cbranch_scc1 .Lmx_wdone
	s_waitcnt vmcnt(0)
.Lmx_wdone:
	s_add_i32 s4, s4, 64
	s_sub_i32 s24, s24, 64
	s_bfe_u32 s100, s4, 0x10006
	s_mul_i32 s100, s100, 0xfffe9200
	v_cndmask_b32_e64 v58, v58, v56, s[76:77]
	v_add_u32_e32 v106, s100, v243
	v_add_u32_e32 v115, s100, v244
	s_cmpk_eq_i32 s4, 0x800
	s_nop 0
	v_cvt_pk_bf16_f32 v6, v6, v7
	v_cvt_pk_bf16_f32 v7, v8, v9
	v_or_b32_e32 v8, s84, v58
	v_ashrrev_i32_e32 v9, 31, v8
	v_lshl_add_u64 v[8:9], v[8:9], 0, s[2:3]
	v_mad_u64_u32 v[14:15], s[8:9], v8, s11, v[54:55]
	v_mad_i32_i24 v15, v9, s11, v15
	global_store_dwordx2 v[14:15], v[6:7], off
	v_add_u32_e32 v6, 16, v56
	v_add_u32_e32 v7, 0x7ef, v57
	v_cndmask_b32_e64 v6, v7, v6, s[76:77]
	v_cvt_pk_bf16_f32 v2, v2, v3
	v_cvt_pk_bf16_f32 v3, v4, v5
	v_or_b32_e32 v4, s84, v6
	v_ashrrev_i32_e32 v5, 31, v4
	v_lshl_add_u64 v[4:5], v[4:5], 0, s[2:3]
	v_mad_u64_u32 v[6:7], s[8:9], v4, s11, v[54:55]
	v_mad_i32_i24 v7, v5, s11, v7
	global_store_dwordx2 v[6:7], v[2:3], off
	s_cbranch_scc1 .LBB0_448
.LBB0_466:
	v_cndmask_b32_e64 v2, 0, 1, s[38:39]
	v_cmp_ne_u32_e64 s[78:79], 1, v2
	s_andn2_b64 vcc, exec, s[38:39]
	s_mov_b64 s[8:9], -1
	s_cbranch_vccnz .LBB0_468
	v_add_u32_e32 v8, s94, v106
	ds_read2st64_b32 v[2:3], v8 offset1:1
	v_add_u32_e32 v16, s94, v105
	ds_read2st64_b32 v[4:5], v8 offset0:2 offset1:3
	ds_read2st64_b32 v[6:7], v8 offset0:4 offset1:5
	ds_read2st64_b32 v[8:9], v8 offset0:6 offset1:7
	s_mov_b64 s[8:9], 0
	s_waitcnt lgkmcnt(0)
	v_lshlrev_b32_e32 v60, 16, v4
	v_lshlrev_b32_e32 v10, 16, v2
	v_mul_f32_e32 v10, 0xbfb8aa3b, v10
	v_exp_f32_e32 v12, v10
	v_and_b32_e32 v2, 0xffff0000, v2
	ds_read2st64_b32 v[10:11], v16 offset1:1
	v_mul_f32_e32 v2, 0xbfb8aa3b, v2
	v_add_f32_e32 v12, 1.0, v12
	v_rcp_f32_e32 v58, v12
	v_exp_f32_e32 v2, v2
	s_waitcnt lgkmcnt(0)
	v_lshlrev_b32_e32 v56, 16, v10
	v_and_b32_e32 v57, 0xffff0000, v10
	v_fma_f32 v10, v45, v58, v140
	v_lshlrev_b32_e32 v58, 16, v3
	v_and_b32_e32 v3, 0xffff0000, v3
	v_add_f32_e32 v2, 1.0, v2
	v_mul_f32_e32 v3, 0xbfb8aa3b, v3
	v_rcp_f32_e32 v2, v2
	v_exp_f32_e32 v3, v3
	v_and_b32_e32 v4, 0xffff0000, v4
	v_mul_f32_e32 v4, 0xbfb8aa3b, v4
	v_fma_f32 v2, v143, v2, v139
	v_add_f32_e32 v3, 1.0, v3
	v_max_f32_e32 v74, 0x358637bd, v2
	v_mul_f32_e32 v58, 0xbfb8aa3b, v58
	v_rcp_f32_e32 v3, v3
	v_exp_f32_e32 v4, v4
	v_log_f32_e32 v2, v74
	v_exp_f32_e32 v58, v58
	v_lshlrev_b32_e32 v62, 16, v5
	v_and_b32_e32 v5, 0xffff0000, v5
	v_fma_f32 v3, v143, v3, v139
	v_add_f32_e32 v4, 1.0, v4
	v_mul_f32_e32 v5, 0xbfb8aa3b, v5
	v_add_f32_e32 v88, 0, v2
	v_add_f32_e32 v2, 1.0, v58
	v_lshlrev_b32_e32 v58, 16, v11
	v_and_b32_e32 v59, 0xffff0000, v11
	v_max_f32_e32 v11, 0x358637bd, v3
	v_mul_f32_e32 v60, 0xbfb8aa3b, v60
	v_rcp_f32_e32 v4, v4
	v_exp_f32_e32 v5, v5
	v_log_f32_e32 v3, v11
	v_exp_f32_e32 v60, v60
	ds_read2st64_b32 v[12:13], v16 offset0:2 offset1:3
	ds_read2st64_b32 v[14:15], v16 offset0:4 offset1:5
	ds_read2st64_b32 v[16:17], v16 offset0:6 offset1:7
	v_lshlrev_b32_e32 v64, 16, v6
	v_and_b32_e32 v6, 0xffff0000, v6
	v_fma_f32 v4, v143, v4, v139
	v_add_f32_e32 v5, 1.0, v5
	v_mul_f32_e32 v6, 0xbfb8aa3b, v6
	v_add_f32_e32 v86, v88, v3
	v_add_f32_e32 v3, 1.0, v60
	s_waitcnt lgkmcnt(0)
	s_cmpk_eq_i32 s4, 0x7c0
	s_cbranch_scc1 .Lmx_q_skip_h
	v_add_u32_e32 v176, s4, v110
	v_add_u32_e32 v177, s24, v121
	v_add_u32_e32 v178, 64, v176
	v_add_u32_e32 v179, 0x7bf, v177
	v_cndmask_b32_e64 v178, v179, v178, s[76:77]
	v_add_u32_e32 v178, s84, v178
	v_mad_i64_i32 v[178:179], s[100:101], v178, s20, v[38:39]
	s_mov_b32 m0, s19
	v_lshl_add_u64 v[178:179], v[178:179], 0, s[80:81]
	global_load_lds_dwordx4 v[178:179], off
	v_add_u32_e32 v176, 0x44, v176
	v_add_u32_e32 v180, 0x7bb, v177
	v_cndmask_b32_e64 v176, v180, v176, s[76:77]
	v_add_u32_e32 v176, s84, v176
	v_mad_i64_i32 v[180:181], s[100:101], v176, s20, v[38:39]
	v_lshl_add_u64 v[180:181], v[180:181], 0, s[80:81]
	s_mov_b32 m0, s85
	s_nop 0
	global_load_lds_dwordx4 v[180:181], off

.LBB0_468:
	s_andn2_b64 vcc, exec, s[8:9]
	s_cbranch_vccnz .LBB0_470
	s_add_i32 s8, s35, s24
	s_add_i32 s5, s95, s4
	s_add_i32 s40, s8, 0x7ff
	s_and_b64 s[8:9], s[76:77], exec
	s_cselect_b32 s5, s5, s40
	v_cvt_f32_i32_e32 v2, s5
	v_add_u32_e32 v10, s83, v105
	v_add_u32_e32 v11, s83, v106
	v_add_u32_e32 v6, s19, v107
	v_mul_f32_e32 v3, v142, v2
	v_mul_f32_e32 v2, v141, v2
	v_mul_f32_e32 v4, 0.15915494, v3
	v_mul_f32_e32 v5, 0.15915494, v2
	v_rndne_f32_e32 v4, v4
	v_fma_f32 v3, v3, 0.15915494, -v4
	v_rndne_f32_e32 v4, v5
	v_fma_f32 v4, v2, 0.15915494, -v4
	v_sin_f32_e32 v2, v3
	v_cos_f32_e32 v8, v3
	v_sin_f32_e32 v3, v4
	v_cos_f32_e32 v9, v4
	v_add_u32_e32 v4, s19, v104
	v_add_u32_e32 v5, s94, v106
	v_add_u32_e32 v7, s94, v115
	v_add_u32_e32 v12, s83, v114
	v_add_u32_e32 v13, s83, v115
	ds_read_b32 v14, v4
	ds_read_b32 v62, v5
	ds_read_b32 v15, v6
	ds_read_b32 v63, v7
	ds_read_b32 v10, v10
	ds_read_b32 v64, v11
	ds_read_b32 v11, v12
	ds_read_b32 v65, v13
	s_waitcnt lgkmcnt(0)
	v_lshlrev_b32_e32 v6, 16, v15
	v_and_b32_e32 v7, 0xffff0000, v15
	v_pk_mul_f32 v[12:13], v[46:47], v[2:3]
	v_lshlrev_b32_e32 v4, 16, v14
	v_and_b32_e32 v5, 0xffff0000, v14
	v_pk_mul_f32 v[6:7], v[12:13], v[6:7]
	v_add_u32_e32 v66, s14, v114
	v_pk_fma_f32 v[56:57], v[8:9], v[4:5], v[6:7]
	s_waitcnt lgkmcnt(3)
	v_lshlrev_b32_e32 v4, 16, v10
	v_and_b32_e32 v5, 0xffff0000, v10
	s_waitcnt lgkmcnt(1)
	v_lshlrev_b32_e32 v6, 16, v11
	v_and_b32_e32 v7, 0xffff0000, v11
	v_pk_mul_f32 v[10:11], v[50:51], v[2:3]
	v_pk_mul_f32 v[2:3], v[48:49], v[2:3]
	v_pk_fma_f32 v[16:17], v[48:49], v[8:9], v[10:11] neg_lo:[0,0,1] neg_hi:[0,0,1]
	v_pk_fma_f32 v[60:61], v[50:51], v[8:9], v[2:3]
	v_mov_b32_e32 v10, v8
	v_pk_mul_f32 v[14:15], v[46:47], v[60:61]
	v_add_u32_e32 v8, s18, v105
	v_pk_mul_f32 v[2:3], v[14:15], v[6:7]
	s_waitcnt lgkmcnt(0)
	v_lshlrev_b32_e32 v7, 16, v65
	v_lshlrev_b32_e32 v6, 16, v62
	v_mov_b32_e32 v11, v14
	v_pk_fma_f32 v[58:59], v[16:17], v[4:5], v[2:3]
	v_lshlrev_b32_e32 v3, 16, v64
	v_lshlrev_b32_e32 v2, 16, v63
	v_pk_mul_f32 v[6:7], v[10:11], v[6:7]
	v_and_b32_e32 v11, 0xffff0000, v64
	v_and_b32_e32 v10, 0xffff0000, v63
	v_and_b32_e32 v63, 0xffff0000, v65
	v_and_b32_e32 v62, 0xffff0000, v62
	v_mov_b32_e32 v14, v9
	v_add_u32_e32 v64, s14, v105
	v_add_u32_e32 v65, s14, v106
	v_pk_mul_f32 v[14:15], v[14:15], v[62:63]
	v_add_u32_e32 v9, s18, v106
	v_add_u32_e32 v62, s18, v114
	v_add_u32_e32 v63, s18, v115
	v_add_u32_e32 v67, s14, v115
	ds_read_b32 v68, v8
	ds_read_b32 v78, v9
	ds_read_b32 v69, v62
	ds_read_b32 v80, v63
	ds_read_b32 v70, v64
	ds_read_b32 v79, v65
	ds_read_b32 v71, v66
	ds_read_b32 v81, v67
	v_pk_mul_f32 v[64:65], v[50:51], v[60:61]
	v_pk_mul_f32 v[60:61], v[48:49], v[60:61]
	v_mov_b32_e32 v4, v12
	v_mov_b32_e32 v5, v16
	v_mov_b32_e32 v12, v13
	v_mov_b32_e32 v13, v17
	v_pk_fma_f32 v[64:65], v[48:49], v[16:17], v[64:65] neg_lo:[0,0,1] neg_hi:[0,0,1]
	v_pk_fma_f32 v[16:17], v[50:51], v[16:17], v[60:61]
	s_waitcnt lgkmcnt(0)
	v_lshlrev_b32_e32 v8, 16, v68
	v_and_b32_e32 v9, 0xffff0000, v68
	s_waitcnt lgkmcnt(5)
	v_lshlrev_b32_e32 v62, 16, v69
	v_and_b32_e32 v63, 0xffff0000, v69
	v_pk_mul_f32 v[66:67], v[46:47], v[16:17]
	v_pk_mul_f32 v[68:69], v[50:51], v[16:17]
	v_pk_mul_f32 v[16:17], v[48:49], v[16:17]
	v_pk_mul_f32 v[60:61], v[66:67], v[62:63]
	v_pk_fma_f32 v[16:17], v[50:51], v[64:65], v[16:17]
	v_pk_fma_f32 v[60:61], v[64:65], v[8:9], v[60:61]
	s_waitcnt lgkmcnt(3)
	v_lshlrev_b32_e32 v8, 16, v70
	v_and_b32_e32 v9, 0xffff0000, v70
	s_waitcnt lgkmcnt(1)
	v_lshlrev_b32_e32 v62, 16, v71
	v_and_b32_e32 v63, 0xffff0000, v71
	v_pk_mul_f32 v[70:71], v[46:47], v[16:17]
	v_pk_fma_f32 v[68:69], v[48:49], v[64:65], v[68:69] neg_lo:[0,0,1] neg_hi:[0,0,1]
	v_pk_mul_f32 v[62:63], v[70:71], v[62:63]
	s_waitcnt lgkmcnt(0)
	v_lshlrev_b32_e32 v73, 16, v81
	v_lshlrev_b32_e32 v72, 16, v80
	v_mov_b32_e32 v76, v66
	v_mov_b32_e32 v77, v70
	v_pk_fma_f32 v[62:63], v[68:69], v[8:9], v[62:63]
	v_lshlrev_b32_e32 v9, 16, v79
	v_lshlrev_b32_e32 v8, 16, v78
	v_pk_mul_f32 v[72:73], v[76:77], v[72:73]
	v_and_b32_e32 v77, 0xffff0000, v79
	v_and_b32_e32 v76, 0xffff0000, v78
	v_and_b32_e32 v79, 0xffff0000, v81
	v_and_b32_e32 v78, 0xffff0000, v80
	v_mov_b32_e32 v70, v67
	v_mov_b32_e32 v74, v64
	v_pk_mul_f32 v[78:79], v[70:71], v[78:79]
	v_add_u32_e32 v64, s13, v105
	v_add_u32_e32 v70, s33, v105
	v_add_u32_e32 v71, s33, v106
	v_mov_b32_e32 v80, v65
	v_add_u32_e32 v65, s13, v106
	v_add_u32_e32 v66, s13, v114
	v_add_u32_e32 v67, s13, v115
	v_add_u32_e32 v82, s33, v114
	v_add_u32_e32 v83, s33, v115
	ds_read_b32 v84, v64
	ds_read_b32 v145, v65
	ds_read_b32 v85, v66
	ds_read_b32 v146, v67
	ds_read_b32 v86, v70
	ds_read_b32 v147, v71
	ds_read_b32 v87, v82
	ds_read_b32 v148, v83
	v_pk_mul_f32 v[70:71], v[50:51], v[16:17]
	v_pk_mul_f32 v[16:17], v[48:49], v[16:17]
	v_mov_b32_e32 v75, v68
	v_pk_fma_f32 v[16:17], v[50:51], v[68:69], v[16:17]
	v_mov_b32_e32 v81, v69
	s_waitcnt lgkmcnt(0)
	v_lshlrev_b32_e32 v64, 16, v84
	v_and_b32_e32 v65, 0xffff0000, v84
	s_waitcnt lgkmcnt(5)
	v_lshlrev_b32_e32 v66, 16, v85
	v_and_b32_e32 v67, 0xffff0000, v85
	v_pk_fma_f32 v[70:71], v[48:49], v[68:69], v[70:71] neg_lo:[0,0,1] neg_hi:[0,0,1]
	v_pk_mul_f32 v[68:69], v[46:47], v[16:17]
	v_pk_mul_f32 v[84:85], v[50:51], v[16:17]
	v_pk_mul_f32 v[16:17], v[48:49], v[16:17]
	v_pk_mul_f32 v[66:67], v[68:69], v[66:67]
	v_pk_fma_f32 v[16:17], v[50:51], v[70:71], v[16:17]
	v_pk_fma_f32 v[64:65], v[70:71], v[64:65], v[66:67]
	s_waitcnt lgkmcnt(3)
	v_lshlrev_b32_e32 v66, 16, v86
	v_and_b32_e32 v67, 0xffff0000, v86
	s_waitcnt lgkmcnt(1)
	v_lshlrev_b32_e32 v82, 16, v87
	v_and_b32_e32 v83, 0xffff0000, v87
	v_pk_mul_f32 v[86:87], v[46:47], v[16:17]
	v_pk_fma_f32 v[84:85], v[48:49], v[70:71], v[84:85] neg_lo:[0,0,1] neg_hi:[0,0,1]
	v_pk_mul_f32 v[82:83], v[86:87], v[82:83]
	s_waitcnt lgkmcnt(0)
	v_lshlrev_b32_e32 v89, 16, v148
	v_lshlrev_b32_e32 v88, 16, v146
	v_mov_b32_e32 v92, v68
	v_mov_b32_e32 v93, v86
	v_pk_fma_f32 v[66:67], v[84:85], v[66:67], v[82:83]
	v_lshlrev_b32_e32 v83, 16, v147
	v_pk_mul_f32 v[88:89], v[92:93], v[88:89]
	v_and_b32_e32 v93, 0xffff0000, v147
	v_and_b32_e32 v147, 0xffff0000, v148
	v_and_b32_e32 v146, 0xffff0000, v146
	v_mov_b32_e32 v86, v69
	v_lshlrev_b32_e32 v82, 16, v145
	v_and_b32_e32 v92, 0xffff0000, v145
	v_pk_mul_f32 v[86:87], v[86:87], v[146:147]
	v_add_u32_e32 v68, s25, v105
	v_add_u32_e32 v145, s10, v105
	v_add_u32_e32 v146, s10, v106
	v_add_u32_e32 v147, s10, v114
	v_mov_b32_e32 v90, v70
	v_mov_b32_e32 v148, v71
	v_add_u32_e32 v69, s25, v106
	v_add_u32_e32 v70, s25, v114
	v_add_u32_e32 v71, s25, v115
	v_add_u32_e32 v150, s10, v115
	ds_read_b32 v151, v68
	ds_read_b32 v152, v69
	ds_read_b32 v153, v70
	ds_read_b32 v154, v71
	ds_read_b32 v145, v145
	ds_read_b32 v155, v146
	ds_read_b32 v157, v147
	ds_read_b32 v160, v150
	v_pk_mul_f32 v[146:147], v[50:51], v[16:17]
	v_pk_mul_f32 v[16:17], v[48:49], v[16:17]
	v_mov_b32_e32 v91, v84
	v_pk_fma_f32 v[16:17], v[50:51], v[84:85], v[16:17]
	v_mov_b32_e32 v149, v85
	v_pk_fma_f32 v[146:147], v[48:49], v[84:85], v[146:147] neg_lo:[0,0,1] neg_hi:[0,0,1]
	v_pk_mul_f32 v[84:85], v[46:47], v[16:17]
	v_pk_mul_f32 v[158:159], v[50:51], v[16:17]
	v_pk_mul_f32 v[16:17], v[48:49], v[16:17]
	s_waitcnt lgkmcnt(0)
	s_cmpk_eq_i32 s4, 0x7c0
	s_cbranch_scc1 .Lmx_q_skip_r
	v_add_u32_e32 v176, s4, v110
	v_add_u32_e32 v177, s24, v121
	v_add_u32_e32 v178, 64, v176
	v_add_u32_e32 v179, 0x7bf, v177
	v_cndmask_b32_e64 v178, v179, v178, s[76:77]
	v_add_u32_e32 v178, s84, v178
	v_mad_i64_i32 v[178:179], s[100:101], v178, s20, v[38:39]
	s_mov_b32 m0, s19
	v_lshl_add_u64 v[178:179], v[178:179], 0, s[80:81]
	global_load_lds_dwordx4 v[178:179], off
	v_add_u32_e32 v176, 0x44, v176
	v_add_u32_e32 v180, 0x7bb, v177
	v_cndmask_b32_e64 v176, v180, v176, s[76:77]
	v_add_u32_e32 v176, s84, v176
	v_mad_i64_i32 v[180:181], s[100:101], v176, s20, v[38:39]
	v_lshl_add_u64 v[180:181], v[180:181], 0, s[80:81]
	s_mov_b32 m0, s85
	s_nop 0
	global_load_lds_dwordx4 v[180:181], off

.LBB0_470:
	v_add_u32_e32 v72, s16, v102
	v_add_u32_e32 v74, s0, v102
	ds_read_u16 v145, v72
	ds_read_u16 v149, v72 offset:128
	ds_read_u16 v146, v72 offset:256
	ds_read_u16 v150, v72 offset:384
	ds_read_u16 v147, v74
	ds_read_u16 v151, v72 offset:640
	ds_read_u16 v148, v72 offset:768
	ds_read_u16 v152, v72 offset:896
	v_add_u32_e32 v72, s17, v103
	ds_write_b64 v72, v[76:77]
	s_waitcnt lgkmcnt(0)
	s_cmpk_eq_i32 s4, 0x7c0
	s_cbranch_scc1 .Lmx_v_skip
	v_add_u32_e32 v176, s4, v119
	v_add_u32_e32 v177, s24, v120
	v_cndmask_b32_e64 v176, v177, v176, s[76:77]
	v_add_u32_e32 v176, s84, v176
	v_mad_i64_i32 v[178:179], s[100:101], v176, s20, v[52:53]
	s_mov_b32 m0, s87
	s_nop 0
	global_load_lds_dwordx4 v[178:179], off
	s_cmpk_ge_i32 s4, 0x780
	s_cbranch_scc1 .Lmx_v_skip
	v_add_u32_e32 v176, s4, v110
	v_add_u32_e32 v177, s24, v121
	v_add_u32_e32 v178, 0x80, v176
	v_add_u32_e32 v179, 0x77f, v177
	v_cndmask_b32_e64 v178, v179, v178, s[76:77]
	v_add_u32_e32 v178, s84, v178
	v_mad_i64_i32 v[178:179], s[100:101], v178, s20, v[38:39]
	v_add_u32_e32 v176, 0x84, v176
	v_add_u32_e32 v180, 0x77b, v177
	v_cndmask_b32_e64 v176, v180, v176, s[76:77]
	v_add_u32_e32 v176, s84, v176
	v_mad_i64_i32 v[180:181], s[100:101], v176, s20, v[38:39]
	v_lshl_add_u64 v[178:179], v[178:179], 0, s[6:7]
	v_lshl_add_u64 v[180:181], v[180:181], 0, s[6:7]
	s_bfe_u32 s100, s4, 0x10006
	s_mul_i32 s100, s100, 0xfffe9200
	s_add_i32 m0, s82, s100
	s_nop 0
	global_load_lds_dwordx4 v[178:179], off
	s_add_i32 m0, s86, s100
	s_nop 0
	global_load_lds_dwordx4 v[180:181], off
